# combine row loop: next row's token-position prefetch read at the loop latch instead of waited right after its load; latch waits vmcnt(8) (only the row's 8 output stores may stay in flight) instead of
# speedup vs baseline: 1.0013x; 1.0005x over previous
; __device__ __forceinline__ void combine_phase(KA A, int l, int wave, int lane, int bid, int G) {
;     ...
;     int4 rn = make_int4(0, 0, 0, 0); int p1n = 0, p2n = 0;
;     { const int row = bid * NWAVES + wave; if (row < MR) { rn = route[row]; p1n = tokpos[row * 2]; p2n = tokpos[row * 2 + 1]; } }
;     for (int row = bid * NWAVES + wave; row < MR; row += G * NWAVES) { const int b = row / TB, s = row % TB;
;         const int4 r = rn; const int p1 = p1n, p2 = p2n;
;         { const int nrow = row + G * NWAVES; if (nrow < MR) { rn = route[nrow]; p1n = tokpos[nrow * 2]; p2n = tokpos[nrow * 2 + 1]; } }
.LBB0_2074:
	s_andn2_b64 vcc, exec, s[20:21]
	s_mov_b32 s18, s15
	s_mov_b32 s6, s14
	s_waitcnt vmcnt(8)
	v_readfirstlane_b32 s4, v232
	v_readfirstlane_b32 s5, v233
	v_mov_b32_e32 v158, v157
	v_mov_b32_e32 v159, v156
	s_cbranch_vccz .LBB0_2182
.LBB0_2075:
	s_add_i32 s14, s6, s24
	s_cmpk_gt_i32 s14, 0x21ff
	s_cselect_b64 s[20:21], -1, 0
	s_and_b64 vcc, exec, s[20:21]
	s_cbranch_vccnz .LBB0_2077
	s_ashr_i32 s15, s14, 31
	s_lshl_b64 s[16:17], s[14:15], 4
	s_add_u32 s16, s12, s16
	s_addc_u32 s17, s13, s17
	s_lshl_b32 s22, s14, 1
	s_ashr_i32 s23, s22, 31
	s_lshl_b64 s[22:23], s[22:23], 2
	s_add_u32 s22, s27, s22
	s_addc_u32 s23, s30, s23
	global_load_dwordx2 v[232:233], v130, s[22:23]
	global_load_dwordx2 v[156:157], v130, s[16:17] offset:4

; __device__ __forceinline__ void combine_phase(KA A, int l, int wave, int lane, int bid, int G) {
;     ...
;         if (s < CTXL) continue;
.LBB0_2181:
	s_mov_b32 s15, s18
	s_waitcnt vmcnt(0)
	s_branch .LBB0_2074
